# attention score phase: straight-line variants per masked-tile count, key operands read ahead, C=0 MFMAs, bias quads read together
# speedup vs baseline: 1.0130x; 1.0003x over previous
.LBB0_373:
	s_sub_i32 s86, 0, s43
	s_sub_i32 s88, 0, s87
	s_cmp_eq_u32 s5, 0
	s_cselect_b32 s89, s79, 0
	s_cmp_eq_u32 s89, 0
	s_cbranch_scc1 .Lat_s0
	s_cmp_eq_u32 s89, 2
	s_cbranch_scc1 .Lat_s2
	s_cmp_eq_u32 s89, 4
	s_cbranch_scc1 .Lat_s4
	s_cmp_eq_u32 s89, 6
	s_cbranch_scc1 .Lat_s6
	s_cmp_eq_u32 s89, 8
	s_cbranch_scc1 .Lat_s8
	s_cmp_gt_i32 s89, 0
	s_cselect_b64 s[16:17], -1, 0
	v_mov_b32_e32 v54, 0
	s_and_b64 vcc, exec, s[16:17]
	v_mov_b32_e32 v66, 0
	v_mov_b32_e32 v67, 0
	v_mov_b32_e32 v68, 0
	v_mov_b32_e32 v69, 0
	s_cbranch_vccnz .LBB0_375
	s_and_b64 s[18:19], s[46:47], exec
	s_cselect_b32 s18, s87, s88
	s_add_i32 s18, s18, 0
	v_add3_u32 v12, s18, v129, v128
	v_add3_u32 v10, s18, v130, v128
	ds_read_b128 v[56:59], v12
	ds_read_b128 v[60:63], v10
	v_mov_b32_e32 v12, v11
	v_mov_b32_e32 v13, v11
	v_mov_b32_e32 v10, v11
	v_mov_b64_e32 v[68:69], v[12:13]
	v_mov_b64_e32 v[66:67], v[10:11]
	s_waitcnt vmcnt(8) lgkmcnt(0)
	s_nop 1
	v_mfma_f32_16x16x128_f8f6f4 v[66:69], v[56:63], v[2:9], v[66:69]

.Lat_join:
	ds_bpermute_b32 v84, v73, v12
	s_waitcnt lgkmcnt(0)
	v_max_f32_e32 v84, v84, v84
	v_max_f32_e32 v12, v12, v84
	v_xor_b32_e32 v84, 32, v158
	v_cmp_lt_i32_e32 vcc, v84, v78
	s_nop 1
	v_cndmask_b32_e32 v78, v158, v84, vcc
	v_lshlrev_b32_e32 v180, 2, v78
	ds_bpermute_b32 v78, v180, v12
	s_andn2_b64 vcc, exec, s[68:69]
	s_waitcnt lgkmcnt(0)
	v_max_f32_e32 v78, v78, v78
	v_max_f32_e32 v78, v12, v78
	v_sub_f32_e32 v2, v2, v78
	v_exp_f32_e32 v2, v2
	v_sub_f32_e32 v3, v3, v78
	v_exp_f32_e32 v3, v3
	v_sub_f32_e32 v4, v4, v78
	v_exp_f32_e32 v4, v4
	v_sub_f32_e32 v5, v5, v78
	v_exp_f32_e32 v5, v5
	v_sub_f32_e32 v6, v6, v78
	v_add_f32_e32 v12, 0, v2
	v_exp_f32_e32 v6, v6
	v_sub_f32_e32 v7, v7, v78
	v_add_f32_e32 v12, v3, v12
	v_exp_f32_e32 v7, v7
	v_sub_f32_e32 v8, v8, v78
	v_add_f32_e32 v12, v4, v12
	v_exp_f32_e32 v8, v8
	v_sub_f32_e32 v9, v9, v78
	v_add_f32_e32 v12, v5, v12
	v_exp_f32_e32 v9, v9
	v_sub_f32_e32 v13, v13, v78
	v_add_f32_e32 v12, v6, v12
	v_exp_f32_e32 v172, v13
	v_sub_f32_e32 v13, v54, v78
	v_add_f32_e32 v12, v7, v12
	v_exp_f32_e32 v173, v13
	v_sub_f32_e32 v13, v55, v78
	v_add_f32_e32 v12, v8, v12
	v_exp_f32_e32 v174, v13
	v_sub_f32_e32 v13, v57, v78
	v_add_f32_e32 v12, v9, v12
	v_exp_f32_e32 v175, v13
	v_sub_f32_e32 v13, v56, v78
	v_add_f32_e32 v12, v172, v12
	v_exp_f32_e32 v176, v13
	v_sub_f32_e32 v13, v66, v78
	v_add_f32_e32 v12, v173, v12
	v_exp_f32_e32 v177, v13
	v_sub_f32_e32 v13, v67, v78
	v_add_f32_e32 v12, v174, v12
	v_exp_f32_e32 v178, v13
	v_sub_f32_e32 v13, v69, v78
	v_add_f32_e32 v12, v175, v12
	v_exp_f32_e32 v179, v13
	v_sub_f32_e32 v13, v58, v78
	v_add_f32_e32 v12, v176, v12
	v_exp_f32_e32 v164, v13
	v_sub_f32_e32 v13, v59, v78
	v_add_f32_e32 v12, v177, v12
	v_exp_f32_e32 v165, v13
	v_sub_f32_e32 v13, v60, v78
	v_add_f32_e32 v12, v178, v12
	v_exp_f32_e32 v166, v13
	v_sub_f32_e32 v13, v61, v78
	v_add_f32_e32 v12, v179, v12
	v_exp_f32_e32 v167, v13
	v_sub_f32_e32 v13, v68, v78
	v_add_f32_e32 v12, v164, v12
	v_exp_f32_e32 v168, v13
	v_sub_f32_e32 v13, v79, v78
	v_add_f32_e32 v12, v165, v12
	v_exp_f32_e32 v169, v13
	v_sub_f32_e32 v13, v80, v78
	v_add_f32_e32 v12, v166, v12
	v_exp_f32_e32 v170, v13
	v_sub_f32_e32 v13, v81, v78
	v_add_f32_e32 v12, v167, v12
	v_exp_f32_e32 v171, v13
	v_sub_f32_e32 v13, v62, v78
	v_add_f32_e32 v12, v168, v12
	v_exp_f32_e32 v88, v13
	v_sub_f32_e32 v13, v63, v78
	v_add_f32_e32 v12, v169, v12
	v_exp_f32_e32 v90, v13
	v_sub_f32_e32 v13, v64, v78
	v_add_f32_e32 v12, v170, v12
	v_exp_f32_e32 v91, v13
	v_sub_f32_e32 v13, v65, v78
	v_add_f32_e32 v12, v171, v12
	v_exp_f32_e32 v92, v13
	v_sub_f32_e32 v10, v10, v78
	v_add_f32_e32 v12, v88, v12
	v_exp_f32_e32 v93, v10
	v_add_f32_e32 v12, v90, v12
	v_add_f32_e32 v12, v91, v12
	v_add_f32_e32 v12, v92, v12
	v_add_f32_e32 v10, v93, v12
	v_sub_f32_e32 v12, v82, v78
	v_exp_f32_e32 v161, v12
	v_sub_f32_e32 v12, v83, v78
	v_exp_f32_e32 v162, v12
	v_sub_f32_e32 v12, v85, v78
	v_exp_f32_e32 v163, v12
	v_sub_f32_e32 v12, v74, v78
	v_exp_f32_e32 v81, v12
	v_sub_f32_e32 v12, v75, v78
	v_add_f32_e32 v10, v161, v10
	v_exp_f32_e32 v82, v12
	v_sub_f32_e32 v12, v76, v78
	v_add_f32_e32 v10, v162, v10
	v_exp_f32_e32 v83, v12
	v_sub_f32_e32 v12, v77, v78
	v_add_f32_e32 v10, v163, v10
	v_exp_f32_e32 v84, v12
	v_sub_f32_e32 v12, v70, v78
	v_add_f32_e32 v10, v81, v10
	v_exp_f32_e32 v85, v12
	v_sub_f32_e32 v12, v71, v78
	v_add_f32_e32 v10, v82, v10
	v_exp_f32_e32 v86, v12
	v_sub_f32_e32 v12, v72, v78
	v_add_f32_e32 v10, v83, v10
	v_exp_f32_e32 v87, v12
	v_sub_f32_e32 v12, v89, v78
	v_add_f32_e32 v10, v84, v10
	v_exp_f32_e32 v89, v12
	v_add_f32_e32 v10, v85, v10
	v_add_f32_e32 v10, v86, v10
	v_add_f32_e32 v10, v87, v10
	v_add_f32_e32 v10, v89, v10
	ds_bpermute_b32 v12, v73, v10
	s_waitcnt lgkmcnt(0)
	v_add_f32_e32 v79, v10, v12
	ds_bpermute_b32 v80, v180, v79
	s_cbranch_vccnz .LBB0_391
	s_and_b64 s[16:17], s[46:47], exec
	s_cselect_b32 s16, s43, s86
	v_add_u32_e32 v10, s16, v157
	v_cvt_pk_bf16_f32 v54, v2, v3
	v_cvt_pk_bf16_f32 v55, v4, v5
	v_cvt_pk_bf16_f32 v56, v6, v7
	v_cvt_pk_bf16_f32 v57, v8, v9
	v_add_u32_e32 v4, v10, v149
	v_add_u32_e32 v8, v10, v150
	v_add_u32_e32 v12, v10, v151
	ds_read_b64_tr_b16 v[2:3], v4
	ds_read_b64_tr_b16 v[4:5], v4 offset:4096
	ds_read_b64_tr_b16 v[6:7], v8
	ds_read_b64_tr_b16 v[8:9], v8 offset:4096
	ds_read_b64_tr_b16 v[58:59], v12
	ds_read_b64_tr_b16 v[60:61], v12 offset:4096
	v_add_u32_e32 v12, v10, v152
	ds_read_b64_tr_b16 v[62:63], v12
	ds_read_b64_tr_b16 v[64:65], v12 offset:4096
	v_add_u32_e32 v12, v10, v153
	ds_read_b64_tr_b16 v[66:67], v12
	ds_read_b64_tr_b16 v[68:69], v12 offset:4096
	v_add_u32_e32 v12, v10, v154
	ds_read_b64_tr_b16 v[70:71], v12
	ds_read_b64_tr_b16 v[72:73], v12 offset:4096
	v_add_u32_e32 v12, v10, v155
	v_add_u32_e32 v10, v10, v156
	ds_read_b64_tr_b16 v[180:181], v12
	ds_read_b64_tr_b16 v[182:183], v12 offset:4096
	ds_read_b64_tr_b16 v[184:185], v10
	ds_read_b64_tr_b16 v[186:187], v10 offset:4096
	s_waitcnt lgkmcnt(14)
	v_mfma_f32_16x16x32_bf16 v[2:5], v[2:5], v[54:57], 0
	s_waitcnt lgkmcnt(12)
	v_mfma_f32_16x16x32_bf16 v[6:9], v[6:9], v[54:57], 0
	s_waitcnt lgkmcnt(10)
	v_mfma_f32_16x16x32_bf16 v[58:61], v[58:61], v[54:57], 0
	s_waitcnt lgkmcnt(8)
	v_mfma_f32_16x16x32_bf16 v[62:65], v[62:65], v[54:57], 0
	s_waitcnt lgkmcnt(6)
	v_mfma_f32_16x16x32_bf16 v[66:69], v[66:69], v[54:57], 0
	s_waitcnt lgkmcnt(4)
	v_mfma_f32_16x16x32_bf16 v[74:77], v[70:73], v[54:57], 0
	s_waitcnt lgkmcnt(2)
	v_mfma_f32_16x16x32_bf16 v[70:73], v[180:183], v[54:57], 0
	s_waitcnt lgkmcnt(0)
	v_mfma_f32_16x16x32_bf16 v[54:57], v[184:187], v[54:57], 0
	s_branch .LBB0_392

.Lat_s0:
	s_and_b64 s[62:63], s[46:47], exec
	s_cselect_b32 s16, s87, s88
	s_and_b64 s[62:63], s[48:49], exec
	s_cselect_b32 s17, s87, s88
	s_and_b64 s[62:63], s[50:51], exec
	s_cselect_b32 s18, s87, s88
	s_and_b64 s[62:63], s[52:53], exec
	s_cselect_b32 s19, s87, s88
	s_and_b64 s[62:63], s[54:55], exec
	s_cselect_b32 s20, s87, s88
	s_and_b64 s[62:63], s[56:57], exec
	s_cselect_b32 s21, s87, s88
	v_add3_u32 v10, s16, v129, v128
	ds_read_b128 v[188:191], v10
	v_add3_u32 v12, s16, v130, v128
	ds_read_b128 v[192:195], v12
	v_add3_u32 v252, s16, v132, v131
	ds_read_b128 v[196:199], v252
	v_add3_u32 v253, s16, v133, v131
	ds_read_b128 v[200:203], v253
	v_add3_u32 v10, s17, v129, v134
	ds_read_b128 v[204:207], v10
	v_add3_u32 v12, s17, v130, v134
	ds_read_b128 v[208:211], v12
	v_add3_u32 v252, s18, v129, v135
	ds_read_b128 v[212:215], v252
	v_add3_u32 v253, s18, v130, v135
	ds_read_b128 v[216:219], v253
	v_add3_u32 v10, s19, v129, v136
	ds_read_b128 v[220:223], v10
	v_add3_u32 v12, s19, v130, v136
	ds_read_b128 v[224:227], v12
	v_add3_u32 v252, s20, v129, v137
	ds_read_b128 v[228:231], v252
	v_add3_u32 v253, s20, v130, v137
	ds_read_b128 v[232:235], v253
	v_add3_u32 v10, s21, v129, v138
	ds_read_b128 v[236:239], v10
	v_add3_u32 v12, s21, v130, v138
	ds_read_b128 v[240:243], v12
	s_waitcnt vmcnt(8)
	s_waitcnt lgkmcnt(12)
	v_mfma_f32_16x16x128_f8f6f4 v[66:69], v[188:195], v[2:9], 0
	v_add3_u32 v252, s21, v129, v139
	ds_read_b128 v[244:247], v252
	v_add3_u32 v253, s21, v130, v139
	ds_read_b128 v[248:251], v253
	s_waitcnt lgkmcnt(12)
	v_mfma_f32_16x16x128_f8f6f4 v[54:57], v[196:203], v[2:9], 0
	v_add3_u32 v10, s88, v129, v140
	ds_read_b128 v[162:165], v10
	v_add3_u32 v12, s88, v130, v140
	ds_read_b128 v[166:169], v12
	s_waitcnt lgkmcnt(12)
	v_mfma_f32_16x16x128_f8f6f4 v[78:81], v[204:211], v[2:9], 0
	v_add3_u32 v252, s88, v129, v141
	ds_read_b128 v[170:173], v252
	v_add3_u32 v253, s88, v130, v141
	ds_read_b128 v[174:177], v253
	s_waitcnt lgkmcnt(12)
	v_mfma_f32_16x16x128_f8f6f4 v[58:61], v[212:219], v[2:9], 0
	s_waitcnt lgkmcnt(10)
	v_mfma_f32_16x16x128_f8f6f4 v[82:85], v[220:227], v[2:9], 0
	s_waitcnt lgkmcnt(8)
	v_mfma_f32_16x16x128_f8f6f4 v[62:65], v[228:235], v[2:9], 0
	s_waitcnt lgkmcnt(6)
	v_mfma_f32_16x16x128_f8f6f4 v[86:89], v[236:243], v[2:9], 0
	s_waitcnt lgkmcnt(4)
	v_mfma_f32_16x16x128_f8f6f4 v[74:77], v[244:251], v[2:9], 0
	s_waitcnt lgkmcnt(2)
	v_mfma_f32_16x16x128_f8f6f4 v[90:93], v[162:169], v[2:9], 0
	s_waitcnt lgkmcnt(0)
	v_mfma_f32_16x16x128_f8f6f4 v[70:73], v[170:177], v[2:9], 0
	ds_read_b128 v[188:191], v111 offset:128
	ds_read_b128 v[192:195], v111 offset:192
	ds_read_b128 v[196:199], v111 offset:256
	ds_read_b128 v[200:203], v111 offset:320
	ds_read_b128 v[204:207], v111 offset:384
	ds_read_b128 v[208:211], v111 offset:448
	ds_read_b128 v[212:215], v111 offset:512
	ds_read_b128 v[216:219], v111 offset:576
	ds_read_b128 v[220:223], v111 offset:640
	ds_read_b128 v[224:227], v111 offset:704
	v_mov_b32_e32 v12, 0xff800000
	s_nop 7
	s_waitcnt lgkmcnt(9)
	v_fmamk_f32 v2, v66, 0x3a0293ee, v188
	v_fmamk_f32 v3, v67, 0x3a0293ee, v189
	v_fmamk_f32 v4, v68, 0x3a0293ee, v190
	v_fmamk_f32 v5, v69, 0x3a0293ee, v191
	v_max3_f32 v12, v12, v2, v3
	v_max3_f32 v12, v12, v4, v5
	s_waitcnt lgkmcnt(8)
	v_fmamk_f32 v6, v54, 0x3a0293ee, v192
	v_fmamk_f32 v7, v55, 0x3a0293ee, v193
	v_fmamk_f32 v8, v56, 0x3a0293ee, v194
	v_fmamk_f32 v9, v57, 0x3a0293ee, v195
	v_max3_f32 v12, v12, v6, v7
	v_max3_f32 v12, v12, v8, v9
	s_waitcnt lgkmcnt(7)
	v_fmamk_f32 v13, v78, 0x3a0293ee, v196
	v_fmamk_f32 v54, v79, 0x3a0293ee, v197
	v_fmamk_f32 v55, v80, 0x3a0293ee, v198
	v_fmamk_f32 v57, v81, 0x3a0293ee, v199
	v_max3_f32 v12, v12, v13, v54
	v_max3_f32 v12, v12, v55, v57
	s_waitcnt lgkmcnt(6)
	v_fmamk_f32 v56, v58, 0x3a0293ee, v200
	v_fmamk_f32 v66, v59, 0x3a0293ee, v201
	v_fmamk_f32 v67, v60, 0x3a0293ee, v202
	v_fmamk_f32 v69, v61, 0x3a0293ee, v203
	v_max3_f32 v12, v12, v56, v66
	v_max3_f32 v12, v12, v67, v69
	s_waitcnt lgkmcnt(5)
	v_fmamk_f32 v58, v82, 0x3a0293ee, v204
	v_fmamk_f32 v59, v83, 0x3a0293ee, v205
	v_fmamk_f32 v60, v84, 0x3a0293ee, v206
	v_fmamk_f32 v61, v85, 0x3a0293ee, v207
	v_max3_f32 v12, v12, v58, v59
	v_max3_f32 v12, v12, v60, v61
	s_waitcnt lgkmcnt(4)
	v_fmamk_f32 v68, v62, 0x3a0293ee, v208
	v_fmamk_f32 v79, v63, 0x3a0293ee, v209
	v_fmamk_f32 v80, v64, 0x3a0293ee, v210
	v_fmamk_f32 v81, v65, 0x3a0293ee, v211
	v_max3_f32 v12, v12, v68, v79
	v_max3_f32 v12, v12, v80, v81
	s_waitcnt lgkmcnt(3)
	v_fmamk_f32 v62, v86, 0x3a0293ee, v212
	v_fmamk_f32 v63, v87, 0x3a0293ee, v213
	v_fmamk_f32 v64, v88, 0x3a0293ee, v214
	v_fmamk_f32 v65, v89, 0x3a0293ee, v215
	v_max3_f32 v12, v12, v62, v63
	v_max3_f32 v12, v12, v64, v65
	s_waitcnt lgkmcnt(2)
	v_fmamk_f32 v10, v74, 0x3a0293ee, v216
	v_fmamk_f32 v82, v75, 0x3a0293ee, v217
	v_fmamk_f32 v83, v76, 0x3a0293ee, v218
	v_fmamk_f32 v85, v77, 0x3a0293ee, v219
	v_max3_f32 v12, v12, v10, v82
	v_max3_f32 v12, v12, v83, v85
	s_waitcnt lgkmcnt(1)
	v_fmamk_f32 v74, v90, 0x3a0293ee, v220
	v_fmamk_f32 v75, v91, 0x3a0293ee, v221
	v_fmamk_f32 v76, v92, 0x3a0293ee, v222
	v_fmamk_f32 v77, v93, 0x3a0293ee, v223
	v_max3_f32 v12, v12, v74, v75
	v_max3_f32 v12, v12, v76, v77
	s_waitcnt lgkmcnt(0)
	v_fmamk_f32 v70, v70, 0x3a0293ee, v224
	v_fmamk_f32 v71, v71, 0x3a0293ee, v225
	v_fmamk_f32 v72, v72, 0x3a0293ee, v226
	v_fmamk_f32 v89, v73, 0x3a0293ee, v227
	v_max3_f32 v12, v12, v70, v71
	v_max3_f32 v12, v12, v72, v89
	v_and_b32_e32 v78, 64, v158
	v_xor_b32_e32 v73, 16, v158
	v_add_u32_e32 v78, 64, v78
	v_cmp_lt_i32_e32 vcc, v73, v78
	s_mov_b32 s16, 0xff800000
	s_mov_b32 s87, s88
	s_mov_b64 s[68:69], -1
	s_mov_b64 s[66:67], -1
	s_mov_b64 s[64:65], -1
	s_mov_b64 s[62:63], -1
	v_cndmask_b32_e32 v73, v158, v73, vcc
	v_lshlrev_b32_e32 v73, 2, v73
	s_branch .Lat_join
.Lat_s2:
	s_and_b64 s[62:63], s[48:49], exec
	s_cselect_b32 s16, s87, s88
	s_and_b64 s[62:63], s[50:51], exec
	s_cselect_b32 s17, s87, s88
	s_and_b64 s[62:63], s[52:53], exec
	s_cselect_b32 s18, s87, s88
	s_and_b64 s[62:63], s[54:55], exec
	s_cselect_b32 s19, s87, s88
	s_and_b64 s[62:63], s[56:57], exec
	s_cselect_b32 s20, s87, s88
	v_add3_u32 v10, s16, v129, v134
	ds_read_b128 v[188:191], v10
	v_add3_u32 v12, s16, v130, v134
	ds_read_b128 v[192:195], v12
	v_add3_u32 v252, s17, v129, v135
	ds_read_b128 v[196:199], v252
	v_add3_u32 v253, s17, v130, v135
	ds_read_b128 v[200:203], v253
	v_add3_u32 v10, s18, v129, v136
	ds_read_b128 v[204:207], v10
	v_add3_u32 v12, s18, v130, v136
	ds_read_b128 v[208:211], v12
	v_add3_u32 v252, s19, v129, v137
	ds_read_b128 v[212:215], v252
	v_add3_u32 v253, s19, v130, v137
	ds_read_b128 v[216:219], v253
	v_add3_u32 v10, s20, v129, v138
	ds_read_b128 v[220:223], v10
	v_add3_u32 v12, s20, v130, v138
	ds_read_b128 v[224:227], v12
	v_add3_u32 v252, s20, v129, v139
	ds_read_b128 v[228:231], v252
	v_add3_u32 v253, s20, v130, v139
	ds_read_b128 v[232:235], v253
	v_add3_u32 v10, s88, v129, v140
	ds_read_b128 v[236:239], v10
	v_add3_u32 v12, s88, v130, v140
	ds_read_b128 v[240:243], v12
	s_waitcnt vmcnt(8)
	s_waitcnt lgkmcnt(12)
	v_mfma_f32_16x16x128_f8f6f4 v[78:81], v[188:195], v[2:9], 0
	v_add3_u32 v252, s88, v129, v141
	ds_read_b128 v[244:247], v252
	v_add3_u32 v253, s88, v130, v141
	ds_read_b128 v[248:251], v253
	s_waitcnt lgkmcnt(12)
	v_mfma_f32_16x16x128_f8f6f4 v[58:61], v[196:203], v[2:9], 0
	s_waitcnt lgkmcnt(10)
	v_mfma_f32_16x16x128_f8f6f4 v[82:85], v[204:211], v[2:9], 0
	s_waitcnt lgkmcnt(8)
	v_mfma_f32_16x16x128_f8f6f4 v[62:65], v[212:219], v[2:9], 0
	s_waitcnt lgkmcnt(6)
	v_mfma_f32_16x16x128_f8f6f4 v[86:89], v[220:227], v[2:9], 0
	s_waitcnt lgkmcnt(4)
	v_mfma_f32_16x16x128_f8f6f4 v[74:77], v[228:235], v[2:9], 0
	s_waitcnt lgkmcnt(2)
	v_mfma_f32_16x16x128_f8f6f4 v[90:93], v[236:243], v[2:9], 0
	s_waitcnt lgkmcnt(0)
	v_mfma_f32_16x16x128_f8f6f4 v[70:73], v[244:251], v[2:9], 0
	ds_read_b128 v[188:191], v111 offset:256
	ds_read_b128 v[192:195], v111 offset:320
	ds_read_b128 v[196:199], v111 offset:384
	ds_read_b128 v[200:203], v111 offset:448
	ds_read_b128 v[204:207], v111 offset:512
	ds_read_b128 v[208:211], v111 offset:576
	ds_read_b128 v[212:215], v111 offset:640
	ds_read_b128 v[216:219], v111 offset:704
	v_mov_b32_e32 v12, 0xff800000
	v_mov_b32_e32 v2, 0xff800000
	v_mov_b32_e32 v3, 0xff800000
	v_mov_b32_e32 v4, 0xff800000
	v_mov_b32_e32 v5, 0xff800000
	v_mov_b32_e32 v6, 0xff800000
	v_mov_b32_e32 v7, 0xff800000
	v_mov_b32_e32 v8, 0xff800000
	v_mov_b32_e32 v9, 0xff800000
	s_nop 7
	s_waitcnt lgkmcnt(7)
	v_fmamk_f32 v13, v78, 0x3a0293ee, v188
	v_fmamk_f32 v54, v79, 0x3a0293ee, v189
	v_fmamk_f32 v55, v80, 0x3a0293ee, v190
	v_fmamk_f32 v57, v81, 0x3a0293ee, v191
	v_max3_f32 v12, v12, v13, v54
	v_max3_f32 v12, v12, v55, v57
	s_waitcnt lgkmcnt(6)
	v_fmamk_f32 v56, v58, 0x3a0293ee, v192
	v_fmamk_f32 v66, v59, 0x3a0293ee, v193
	v_fmamk_f32 v67, v60, 0x3a0293ee, v194
	v_fmamk_f32 v69, v61, 0x3a0293ee, v195
	v_max3_f32 v12, v12, v56, v66
	v_max3_f32 v12, v12, v67, v69
	s_waitcnt lgkmcnt(5)
	v_fmamk_f32 v58, v82, 0x3a0293ee, v196
	v_fmamk_f32 v59, v83, 0x3a0293ee, v197
	v_fmamk_f32 v60, v84, 0x3a0293ee, v198
	v_fmamk_f32 v61, v85, 0x3a0293ee, v199
	v_max3_f32 v12, v12, v58, v59
	v_max3_f32 v12, v12, v60, v61
	s_waitcnt lgkmcnt(4)
	v_fmamk_f32 v68, v62, 0x3a0293ee, v200
	v_fmamk_f32 v79, v63, 0x3a0293ee, v201
	v_fmamk_f32 v80, v64, 0x3a0293ee, v202
	v_fmamk_f32 v81, v65, 0x3a0293ee, v203
	v_max3_f32 v12, v12, v68, v79
	v_max3_f32 v12, v12, v80, v81
	s_waitcnt lgkmcnt(3)
	v_fmamk_f32 v62, v86, 0x3a0293ee, v204
	v_fmamk_f32 v63, v87, 0x3a0293ee, v205
	v_fmamk_f32 v64, v88, 0x3a0293ee, v206
	v_fmamk_f32 v65, v89, 0x3a0293ee, v207
	v_max3_f32 v12, v12, v62, v63
	v_max3_f32 v12, v12, v64, v65
	s_waitcnt lgkmcnt(2)
	v_fmamk_f32 v10, v74, 0x3a0293ee, v208
	v_fmamk_f32 v82, v75, 0x3a0293ee, v209
	v_fmamk_f32 v83, v76, 0x3a0293ee, v210
	v_fmamk_f32 v85, v77, 0x3a0293ee, v211
	v_max3_f32 v12, v12, v10, v82
	v_max3_f32 v12, v12, v83, v85
	s_waitcnt lgkmcnt(1)
	v_fmamk_f32 v74, v90, 0x3a0293ee, v212
	v_fmamk_f32 v75, v91, 0x3a0293ee, v213
	v_fmamk_f32 v76, v92, 0x3a0293ee, v214
	v_fmamk_f32 v77, v93, 0x3a0293ee, v215
	v_max3_f32 v12, v12, v74, v75
	v_max3_f32 v12, v12, v76, v77
	s_waitcnt lgkmcnt(0)
	v_fmamk_f32 v70, v70, 0x3a0293ee, v216
	v_fmamk_f32 v71, v71, 0x3a0293ee, v217
	v_fmamk_f32 v72, v72, 0x3a0293ee, v218
	v_fmamk_f32 v89, v73, 0x3a0293ee, v219
	v_max3_f32 v12, v12, v70, v71
	v_max3_f32 v12, v12, v72, v89
	v_and_b32_e32 v78, 64, v158
	v_xor_b32_e32 v73, 16, v158
	v_add_u32_e32 v78, 64, v78
	v_cmp_lt_i32_e32 vcc, v73, v78
	s_mov_b32 s16, 0xff800000
	s_mov_b32 s87, s88
	s_mov_b64 s[68:69], 0
	s_mov_b64 s[66:67], -1
	s_mov_b64 s[64:65], -1
	s_mov_b64 s[62:63], -1
	v_cndmask_b32_e32 v73, v158, v73, vcc
	v_lshlrev_b32_e32 v73, 2, v73
	s_branch .Lat_join
.Lat_s4:
	s_and_b64 s[62:63], s[52:53], exec
	s_cselect_b32 s16, s87, s88
	s_and_b64 s[62:63], s[54:55], exec
	s_cselect_b32 s17, s87, s88
	s_and_b64 s[62:63], s[56:57], exec
	s_cselect_b32 s18, s87, s88
	v_add3_u32 v10, s16, v129, v136
	ds_read_b128 v[188:191], v10
	v_add3_u32 v12, s16, v130, v136
	ds_read_b128 v[192:195], v12
	v_add3_u32 v252, s17, v129, v137
	ds_read_b128 v[196:199], v252
	v_add3_u32 v253, s17, v130, v137
	ds_read_b128 v[200:203], v253
	v_add3_u32 v10, s18, v129, v138
	ds_read_b128 v[204:207], v10
	v_add3_u32 v12, s18, v130, v138
	ds_read_b128 v[208:211], v12
	v_add3_u32 v252, s18, v129, v139
	ds_read_b128 v[212:215], v252
	v_add3_u32 v253, s18, v130, v139
	ds_read_b128 v[216:219], v253
	v_add3_u32 v10, s88, v129, v140
	ds_read_b128 v[220:223], v10
	v_add3_u32 v12, s88, v130, v140
	ds_read_b128 v[224:227], v12
	v_add3_u32 v252, s88, v129, v141
	ds_read_b128 v[228:231], v252
	v_add3_u32 v253, s88, v130, v141
	ds_read_b128 v[232:235], v253
	s_waitcnt vmcnt(8)
	s_waitcnt lgkmcnt(10)
	v_mfma_f32_16x16x128_f8f6f4 v[82:85], v[188:195], v[2:9], 0
	s_waitcnt lgkmcnt(8)
	v_mfma_f32_16x16x128_f8f6f4 v[62:65], v[196:203], v[2:9], 0
	s_waitcnt lgkmcnt(6)
	v_mfma_f32_16x16x128_f8f6f4 v[86:89], v[204:211], v[2:9], 0
	s_waitcnt lgkmcnt(4)
	v_mfma_f32_16x16x128_f8f6f4 v[74:77], v[212:219], v[2:9], 0
	s_waitcnt lgkmcnt(2)
	v_mfma_f32_16x16x128_f8f6f4 v[90:93], v[220:227], v[2:9], 0
	s_waitcnt lgkmcnt(0)
	v_mfma_f32_16x16x128_f8f6f4 v[70:73], v[228:235], v[2:9], 0
	ds_read_b128 v[188:191], v111 offset:384
	ds_read_b128 v[192:195], v111 offset:448
	ds_read_b128 v[196:199], v111 offset:512
	ds_read_b128 v[200:203], v111 offset:576
	ds_read_b128 v[204:207], v111 offset:640
	ds_read_b128 v[208:211], v111 offset:704
	v_mov_b32_e32 v12, 0xff800000
	v_mov_b32_e32 v2, 0xff800000
	v_mov_b32_e32 v3, 0xff800000
	v_mov_b32_e32 v4, 0xff800000
	v_mov_b32_e32 v5, 0xff800000
	v_mov_b32_e32 v6, 0xff800000
	v_mov_b32_e32 v7, 0xff800000
	v_mov_b32_e32 v8, 0xff800000
	v_mov_b32_e32 v9, 0xff800000
	v_mov_b32_e32 v13, 0xff800000
	v_mov_b32_e32 v54, 0xff800000
	v_mov_b32_e32 v55, 0xff800000
	v_mov_b32_e32 v57, 0xff800000
	v_mov_b32_e32 v56, 0xff800000
	v_mov_b32_e32 v66, 0xff800000
	v_mov_b32_e32 v67, 0xff800000
	v_mov_b32_e32 v69, 0xff800000
	s_nop 7
	s_waitcnt lgkmcnt(5)
	v_fmamk_f32 v58, v82, 0x3a0293ee, v188
	v_fmamk_f32 v59, v83, 0x3a0293ee, v189
	v_fmamk_f32 v60, v84, 0x3a0293ee, v190
	v_fmamk_f32 v61, v85, 0x3a0293ee, v191
	v_max3_f32 v12, v12, v58, v59
	v_max3_f32 v12, v12, v60, v61
	s_waitcnt lgkmcnt(4)
	v_fmamk_f32 v68, v62, 0x3a0293ee, v192
	v_fmamk_f32 v79, v63, 0x3a0293ee, v193
	v_fmamk_f32 v80, v64, 0x3a0293ee, v194
	v_fmamk_f32 v81, v65, 0x3a0293ee, v195
	v_max3_f32 v12, v12, v68, v79
	v_max3_f32 v12, v12, v80, v81
	s_waitcnt lgkmcnt(3)
	v_fmamk_f32 v62, v86, 0x3a0293ee, v196
	v_fmamk_f32 v63, v87, 0x3a0293ee, v197
	v_fmamk_f32 v64, v88, 0x3a0293ee, v198
	v_fmamk_f32 v65, v89, 0x3a0293ee, v199
	v_max3_f32 v12, v12, v62, v63
	v_max3_f32 v12, v12, v64, v65
	s_waitcnt lgkmcnt(2)
	v_fmamk_f32 v10, v74, 0x3a0293ee, v200
	v_fmamk_f32 v82, v75, 0x3a0293ee, v201
	v_fmamk_f32 v83, v76, 0x3a0293ee, v202
	v_fmamk_f32 v85, v77, 0x3a0293ee, v203
	v_max3_f32 v12, v12, v10, v82
	v_max3_f32 v12, v12, v83, v85
	s_waitcnt lgkmcnt(1)
	v_fmamk_f32 v74, v90, 0x3a0293ee, v204
	v_fmamk_f32 v75, v91, 0x3a0293ee, v205
	v_fmamk_f32 v76, v92, 0x3a0293ee, v206
	v_fmamk_f32 v77, v93, 0x3a0293ee, v207
	v_max3_f32 v12, v12, v74, v75
	v_max3_f32 v12, v12, v76, v77
	s_waitcnt lgkmcnt(0)
	v_fmamk_f32 v70, v70, 0x3a0293ee, v208
	v_fmamk_f32 v71, v71, 0x3a0293ee, v209
	v_fmamk_f32 v72, v72, 0x3a0293ee, v210
	v_fmamk_f32 v89, v73, 0x3a0293ee, v211
	v_max3_f32 v12, v12, v70, v71
	v_max3_f32 v12, v12, v72, v89
	v_and_b32_e32 v78, 64, v158
	v_xor_b32_e32 v73, 16, v158
	v_add_u32_e32 v78, 64, v78
	v_cmp_lt_i32_e32 vcc, v73, v78
	s_mov_b32 s16, 0xff800000
	s_mov_b32 s87, s88
	s_mov_b64 s[68:69], 0
	s_mov_b64 s[66:67], 0
	s_mov_b64 s[64:65], -1
	s_mov_b64 s[62:63], -1
	v_cndmask_b32_e32 v73, v158, v73, vcc
	v_lshlrev_b32_e32 v73, 2, v73
	s_branch .Lat_join
.Lat_s6:
	s_and_b64 s[62:63], s[56:57], exec
	s_cselect_b32 s16, s87, s88
	v_add3_u32 v10, s16, v129, v138
	ds_read_b128 v[188:191], v10
	v_add3_u32 v12, s16, v130, v138
	ds_read_b128 v[192:195], v12
	v_add3_u32 v252, s16, v129, v139
	ds_read_b128 v[196:199], v252
	v_add3_u32 v253, s16, v130, v139
	ds_read_b128 v[200:203], v253
	v_add3_u32 v10, s88, v129, v140
	ds_read_b128 v[204:207], v10
	v_add3_u32 v12, s88, v130, v140
	ds_read_b128 v[208:211], v12
	v_add3_u32 v252, s88, v129, v141
	ds_read_b128 v[212:215], v252
	v_add3_u32 v253, s88, v130, v141
	ds_read_b128 v[216:219], v253
	s_waitcnt vmcnt(8)
	s_waitcnt lgkmcnt(6)
	v_mfma_f32_16x16x128_f8f6f4 v[86:89], v[188:195], v[2:9], 0
	s_waitcnt lgkmcnt(4)
	v_mfma_f32_16x16x128_f8f6f4 v[74:77], v[196:203], v[2:9], 0
	s_waitcnt lgkmcnt(2)
	v_mfma_f32_16x16x128_f8f6f4 v[90:93], v[204:211], v[2:9], 0
	s_waitcnt lgkmcnt(0)
	v_mfma_f32_16x16x128_f8f6f4 v[70:73], v[212:219], v[2:9], 0
	ds_read_b128 v[188:191], v111 offset:512
	ds_read_b128 v[192:195], v111 offset:576
	ds_read_b128 v[196:199], v111 offset:640
	ds_read_b128 v[200:203], v111 offset:704
	v_mov_b32_e32 v12, 0xff800000
	v_mov_b32_e32 v2, 0xff800000
	v_mov_b32_e32 v3, 0xff800000
	v_mov_b32_e32 v4, 0xff800000
	v_mov_b32_e32 v5, 0xff800000
	v_mov_b32_e32 v6, 0xff800000
	v_mov_b32_e32 v7, 0xff800000
	v_mov_b32_e32 v8, 0xff800000
	v_mov_b32_e32 v9, 0xff800000
	v_mov_b32_e32 v13, 0xff800000
	v_mov_b32_e32 v54, 0xff800000
	v_mov_b32_e32 v55, 0xff800000
	v_mov_b32_e32 v57, 0xff800000
	v_mov_b32_e32 v56, 0xff800000
	v_mov_b32_e32 v66, 0xff800000
	v_mov_b32_e32 v67, 0xff800000
	v_mov_b32_e32 v69, 0xff800000
	v_mov_b32_e32 v58, 0xff800000
	v_mov_b32_e32 v59, 0xff800000
	v_mov_b32_e32 v60, 0xff800000
	v_mov_b32_e32 v61, 0xff800000
	v_mov_b32_e32 v68, 0xff800000
	v_mov_b32_e32 v79, 0xff800000
	v_mov_b32_e32 v80, 0xff800000
	v_mov_b32_e32 v81, 0xff800000
	s_nop 7
	s_waitcnt lgkmcnt(3)
	v_fmamk_f32 v62, v86, 0x3a0293ee, v188
	v_fmamk_f32 v63, v87, 0x3a0293ee, v189
	v_fmamk_f32 v64, v88, 0x3a0293ee, v190
	v_fmamk_f32 v65, v89, 0x3a0293ee, v191
	v_max3_f32 v12, v12, v62, v63
	v_max3_f32 v12, v12, v64, v65
	s_waitcnt lgkmcnt(2)
	v_fmamk_f32 v10, v74, 0x3a0293ee, v192
	v_fmamk_f32 v82, v75, 0x3a0293ee, v193
	v_fmamk_f32 v83, v76, 0x3a0293ee, v194
	v_fmamk_f32 v85, v77, 0x3a0293ee, v195
	v_max3_f32 v12, v12, v10, v82
	v_max3_f32 v12, v12, v83, v85
	s_waitcnt lgkmcnt(1)
	v_fmamk_f32 v74, v90, 0x3a0293ee, v196
	v_fmamk_f32 v75, v91, 0x3a0293ee, v197
	v_fmamk_f32 v76, v92, 0x3a0293ee, v198
	v_fmamk_f32 v77, v93, 0x3a0293ee, v199
	v_max3_f32 v12, v12, v74, v75
	v_max3_f32 v12, v12, v76, v77
	s_waitcnt lgkmcnt(0)
	v_fmamk_f32 v70, v70, 0x3a0293ee, v200
	v_fmamk_f32 v71, v71, 0x3a0293ee, v201
	v_fmamk_f32 v72, v72, 0x3a0293ee, v202
	v_fmamk_f32 v89, v73, 0x3a0293ee, v203
	v_max3_f32 v12, v12, v70, v71
	v_max3_f32 v12, v12, v72, v89
	v_and_b32_e32 v78, 64, v158
	v_xor_b32_e32 v73, 16, v158
	v_add_u32_e32 v78, 64, v78
	v_cmp_lt_i32_e32 vcc, v73, v78
	s_mov_b32 s16, 0xff800000
	s_mov_b32 s87, s88
	s_mov_b64 s[68:69], 0
	s_mov_b64 s[66:67], 0
	s_mov_b64 s[64:65], 0
	s_mov_b64 s[62:63], -1
	v_cndmask_b32_e32 v73, v158, v73, vcc
	v_lshlrev_b32_e32 v73, 2, v73
	s_branch .Lat_join
.Lat_s8:
	v_add3_u32 v10, s88, v129, v140
	ds_read_b128 v[188:191], v10
	v_add3_u32 v12, s88, v130, v140
	ds_read_b128 v[192:195], v12
	v_add3_u32 v252, s88, v129, v141
	ds_read_b128 v[196:199], v252
	v_add3_u32 v253, s88, v130, v141
	ds_read_b128 v[200:203], v253
	s_waitcnt vmcnt(8)
	s_waitcnt lgkmcnt(2)
	v_mfma_f32_16x16x128_f8f6f4 v[90:93], v[188:195], v[2:9], 0
	s_waitcnt lgkmcnt(0)
	v_mfma_f32_16x16x128_f8f6f4 v[70:73], v[196:203], v[2:9], 0
	ds_read_b128 v[188:191], v111 offset:640
	ds_read_b128 v[192:195], v111 offset:704
	v_mov_b32_e32 v12, 0xff800000
	v_mov_b32_e32 v2, 0xff800000
	v_mov_b32_e32 v3, 0xff800000
	v_mov_b32_e32 v4, 0xff800000
	v_mov_b32_e32 v5, 0xff800000
	v_mov_b32_e32 v6, 0xff800000
	v_mov_b32_e32 v7, 0xff800000
	v_mov_b32_e32 v8, 0xff800000
	v_mov_b32_e32 v9, 0xff800000
	v_mov_b32_e32 v13, 0xff800000
	v_mov_b32_e32 v54, 0xff800000
	v_mov_b32_e32 v55, 0xff800000
	v_mov_b32_e32 v57, 0xff800000
	v_mov_b32_e32 v56, 0xff800000
	v_mov_b32_e32 v66, 0xff800000
	v_mov_b32_e32 v67, 0xff800000
	v_mov_b32_e32 v69, 0xff800000
	v_mov_b32_e32 v58, 0xff800000
	v_mov_b32_e32 v59, 0xff800000
	v_mov_b32_e32 v60, 0xff800000
	v_mov_b32_e32 v61, 0xff800000
	v_mov_b32_e32 v68, 0xff800000
	v_mov_b32_e32 v79, 0xff800000
	v_mov_b32_e32 v80, 0xff800000
	v_mov_b32_e32 v81, 0xff800000
	v_mov_b32_e32 v62, 0xff800000
	v_mov_b32_e32 v63, 0xff800000
	v_mov_b32_e32 v64, 0xff800000
	v_mov_b32_e32 v65, 0xff800000
	v_mov_b32_e32 v10, 0xff800000
	v_mov_b32_e32 v82, 0xff800000
	v_mov_b32_e32 v83, 0xff800000
	v_mov_b32_e32 v85, 0xff800000
	s_nop 7
	s_waitcnt lgkmcnt(1)
	v_fmamk_f32 v74, v90, 0x3a0293ee, v188
	v_fmamk_f32 v75, v91, 0x3a0293ee, v189
	v_fmamk_f32 v76, v92, 0x3a0293ee, v190
	v_fmamk_f32 v77, v93, 0x3a0293ee, v191
	v_max3_f32 v12, v12, v74, v75
	v_max3_f32 v12, v12, v76, v77
	s_waitcnt lgkmcnt(0)
	v_fmamk_f32 v70, v70, 0x3a0293ee, v192
	v_fmamk_f32 v71, v71, 0x3a0293ee, v193
	v_fmamk_f32 v72, v72, 0x3a0293ee, v194
	v_fmamk_f32 v89, v73, 0x3a0293ee, v195
	v_max3_f32 v12, v12, v70, v71
	v_max3_f32 v12, v12, v72, v89
	v_and_b32_e32 v78, 64, v158
	v_xor_b32_e32 v73, 16, v158
	v_add_u32_e32 v78, 64, v78
	v_cmp_lt_i32_e32 vcc, v73, v78
	s_mov_b32 s16, 0xff800000
	s_mov_b32 s87, s88
	s_mov_b64 s[68:69], 0
	s_mov_b64 s[66:67], 0
	s_mov_b64 s[64:65], 0
	s_mov_b64 s[62:63], 0
	v_cndmask_b32_e32 v73, v158, v73, vcc
	v_lshlrev_b32_e32 v73, 2, v73
	s_branch .Lat_join
